# speedup vs baseline: 1.0076x; 1.0076x over previous
_Z13gemm8p_kernel5GArgs:
	s_add_i32 s3, s2, 0x120
	s_sub_i32 s26, s2, 0xc0
	s_cmp_lt_u32 s2, 0xc0
	s_cselect_b32 s2, s3, s26
	s_load_dwordx4 s[20:23], s[0:1], 0x80
	s_load_dwordx8 s[4:11], s[0:1], 0x0
	s_load_dwordx8 s[12:19], s[0:1], 0x48
	s_load_dwordx2 s[24:25], s[0:1], 0x38
	v_and_b32_e32 v2, 32, v0
	s_waitcnt lgkmcnt(0)
	s_cmp_lt_i32 s2, s22
	s_cselect_b64 s[26:27], -1, 0
	s_and_b64 s[28:29], s[26:27], exec
	s_cselect_b32 s12, s4, s12
	s_cselect_b32 s3, s25, s21
	s_cselect_b32 s4, 0, s22
	s_cselect_b32 s13, s5, s13
	s_cselect_b32 s7, s7, s15
	s_cselect_b32 s14, s6, s14
	s_sub_i32 s2, s2, s4
	s_and_b32 s4, s2, 7
	s_lshl_b32 s5, s3, 2
	s_mul_i32 s4, s4, s5
	s_lshr_b32 s5, s2, 3
	s_add_i32 s2, s4, s5
	s_lshl_b32 s5, s3, 4
	s_cmp_ge_u32 s2, s5
	s_cselect_b32 s6, s5, 0
	s_cselect_b32 s5, 16, 0
	s_sub_i32 s2, s2, s6
	s_lshr_b32 s4, s2, 4
	s_and_b32 s2, s2, 15
	s_add_i32 s15, s2, s5
	v_bfe_u32 v155, v0, 2, 4
	v_mov_b32_e32 v3, 0
	v_lshrrev_b32_e32 v6, 3, v0
	s_branch .Lgemm_idx_pad_end
	s_nop 0
	s_nop 0
	s_nop 0
	s_nop 0
	s_nop 0
	s_nop 0
	s_nop 0
	s_nop 0
	s_nop 0
	s_nop 0
	s_nop 0
	s_nop 0
	s_nop 0
	s_nop 0
	s_nop 0
	s_nop 0
	s_nop 0
	s_nop 0
	s_nop 0
	s_nop 0
	s_nop 0
	s_nop 0
	s_nop 0
	s_nop 0
	s_nop 0
	s_nop 0
	s_nop 0
	s_nop 0
	s_nop 0
	s_nop 0
	s_nop 0
	s_nop 0
	s_nop 0
	s_nop 0
	s_nop 0
	s_nop 0
	s_nop 0
	s_nop 0
	s_nop 0
	s_nop 0
	s_nop 0
	s_nop 0
	s_nop 0
	s_nop 0
	s_nop 0
	s_nop 0
	s_nop 0
	s_nop 0
	s_nop 0
	s_nop 0
	s_nop 0
	s_nop 0
	s_nop 0
	s_nop 0
	s_nop 0
	s_nop 0
	s_nop 0
	s_nop 0
	s_nop 0
	s_nop 0
